# mfma5 attention (dilation 16): waves owning the always-masked window rows stop re-loading them after both LDS buffers are primed
# baseline (speedup 1.0000x reference)
; #define AT_SU(s_) (2 * AT_P((s_) >> 1) + ((s_) & 1))
; #define AT_OK(s_) ((s_) < ns && AT_P((s_) >> 1) < NP)
; #define AT_SU(s_) (2 * AT_P((s_) >> 1) + ((s_) & 1))
; __device__ __forceinline__ void attn_group_mfma5(const bf16* QK, const float* bias2g, int ldil, int first, bf16* OACC, float* LSE, LAS unsigned char* lds, const int tid, const int bid, const int G) {
;     ...
;         if (!AT_OK(s)) break;
;         const bool more = AT_OK(s + 1);
;         if (more) { bv = AT_BIAS(AT_SU(s + 1)); AT_DMA(AT_SU(s + 1), (s + 1) & 1); }
.LBB0_206:
	v_readlane_b32 s98, v254, 38
	s_nop 1
	s_add_i32 s98, s98, 2
	s_and_b32 s98, s98, 7
	s_cmp_lt_u32 s98, 4
	s_cselect_b32 s98, 1, 0
	s_cmp_eq_u32 s43, 4
	s_cselect_b32 s98, s98, 0
	s_cmp_gt_u32 s0, 0
	s_cselect_b32 s98, s98, 0
	s_lshl_b32 s36, s60, 1
	s_and_b32 s42, s77, 1
	s_or_b32 s36, s36, s42
	s_and_b32 s37, s36, s48
	s_lshl_b32 s37, s37, 7
	s_ashr_i32 s36, s36, s39
	s_sub_i32 s71, s37, 64
	s_ashr_i32 s37, s60, 3
	s_and_b32 s70, s36, s49
	s_bfe_u32 s36, s60, 0x40003
	s_and_b32 s37, s37, -16
	v_mov_b32_e32 v18, v66
	s_or_b32 s36, s37, s36
	s_ashr_i32 s37, s36, 31
	v_ashrrev_i32_e32 v19, 3, v18
	s_add_i32 s60, s71, s63
	s_lshl_b64 s[36:37], s[36:37], s43
	v_add_u32_e32 v0, s60, v19
	s_or_b32 s36, s36, s70
	v_min_i32_e32 v1, s57, v0
	v_cmp_lt_i32_e32 vcc, -1, v0
	s_lshl_b64 s[36:37], s[36:37], s58
	s_mul_i32 s42, s42, 0x10300
	v_cndmask_b32_e32 v2, 0, v1, vcc
	v_lshl_add_u64 v[0:1], s[36:37], 0, v[2:3]
	v_lshrrev_b32_e32 v2, 1, v19
	v_xor_b32_e32 v2, v2, v18
	v_lshlrev_b64 v[0:1], 7, v[0:1]
	v_lshlrev_b32_e32 v2, 4, v2
	s_add_i32 s42, s42, 0
	v_lshl_add_u64 v[0:1], s[80:81], 0, v[0:1]
	v_and_b32_e32 v2, 0x70, v2
	v_lshl_add_u64 v[0:1], v[0:1], 0, v[2:3]
	s_mov_b64 s[16:17], 0x8000000
	s_mov_b64 s[18:19], 0x4000000
	s_add_i32 s60, s42, s59
	v_lshl_add_u64 v[12:13], v[0:1], 0, s[16:17]
	v_lshl_add_u64 v[0:1], v[0:1], 0, s[18:19]
	s_mov_b32 m0, s60
	s_add_i32 s70, s71, s68
	s_cmp_eq_u32 s98, 1
	s_cbranch_scc1 .Lm5s_0
	global_load_lds_dwordx4 v[0:1], off nt
.Lm5s_0:
	v_add_u32_e32 v0, s70, v19
	v_min_i32_e32 v1, s57, v0
	v_cmp_lt_i32_e32 vcc, -1, v0
	s_add_i32 m0, s42, s72
	s_add_i32 s70, s71, s73
	v_cndmask_b32_e32 v2, 0, v1, vcc
	v_lshl_add_u64 v[0:1], s[36:37], 0, v[2:3]
	v_add_u32_e32 v2, s68, v19
	v_lshrrev_b32_e32 v2, 1, v2
	v_xor_b32_e32 v2, v2, v18
	v_lshlrev_b64 v[0:1], 7, v[0:1]
	v_lshlrev_b32_e32 v2, 4, v2
	v_lshl_add_u64 v[0:1], s[80:81], 0, v[0:1]
	v_and_b32_e32 v2, 0x70, v2
	v_lshl_add_u64 v[0:1], v[0:1], 0, v[2:3]
	v_lshl_add_u64 v[14:15], v[0:1], 0, s[16:17]
	v_lshl_add_u64 v[0:1], v[0:1], 0, s[18:19]
	s_cmp_eq_u32 s98, 1
	s_cbranch_scc1 .Lm5s_1
	global_load_lds_dwordx4 v[0:1], off nt
.Lm5s_1:
	v_add_u32_e32 v0, s70, v19
	v_min_i32_e32 v1, s57, v0
	v_cmp_lt_i32_e32 vcc, -1, v0
	s_add_i32 m0, s42, s74
	s_add_i32 s71, s71, s75
	v_cndmask_b32_e32 v2, 0, v1, vcc
	v_lshl_add_u64 v[0:1], s[36:37], 0, v[2:3]
	v_add_u32_e32 v2, s73, v19
	v_lshrrev_b32_e32 v2, 1, v2
	v_xor_b32_e32 v2, v2, v18
	v_lshlrev_b64 v[0:1], 7, v[0:1]
	v_lshlrev_b32_e32 v2, 4, v2
	v_lshl_add_u64 v[0:1], s[80:81], 0, v[0:1]
	v_and_b32_e32 v2, 0x70, v2
	v_lshl_add_u64 v[0:1], v[0:1], 0, v[2:3]
	v_lshl_add_u64 v[16:17], v[0:1], 0, s[16:17]
	v_lshl_add_u64 v[0:1], v[0:1], 0, s[18:19]
	s_cmp_eq_u32 s98, 1
	s_cbranch_scc1 .Lm5s_2
	global_load_lds_dwordx4 v[0:1], off nt
.Lm5s_2:
	v_add_u32_e32 v0, s71, v19
	v_min_i32_e32 v1, s57, v0
	v_cmp_lt_i32_e32 vcc, -1, v0
	s_add_i32 m0, s42, s76
	s_movk_i32 s70, 0xff
	v_cndmask_b32_e32 v2, 0, v1, vcc
	v_lshl_add_u64 v[0:1], s[36:37], 0, v[2:3]
	v_add_u32_e32 v2, s75, v19
	v_lshrrev_b32_e32 v2, 1, v2
	v_xor_b32_e32 v2, v2, v18
	v_lshlrev_b64 v[0:1], 7, v[0:1]
	v_lshlrev_b32_e32 v2, 4, v2
	v_lshl_add_u64 v[0:1], s[80:81], 0, v[0:1]
	v_and_b32_e32 v2, 0x70, v2
	v_lshl_add_u64 v[0:1], v[0:1], 0, v[2:3]
	v_lshl_add_u64 v[18:19], v[0:1], 0, s[16:17]
	v_lshl_add_u64 v[0:1], v[0:1], 0, s[18:19]
	s_cmp_eq_u32 s98, 1
	s_cbranch_scc1 .Lm5s_3
	global_load_lds_dwordx4 v[0:1], off nt
.Lm5s_3:
	s_add_i32 m0, s60, 0x8000
	s_movk_i32 s71, 0xdf
	s_cmp_eq_u32 s98, 1
	s_cbranch_scc1 .Lm5s_4
	global_load_lds_dwordx4 v[12:13], off nt
.Lm5s_4:
	s_add_i32 m0, s60, 0x8400
	s_mov_b64 s[16:17], s[20:21]
	s_cmp_eq_u32 s98, 1
	s_cbranch_scc1 .Lm5s_5
	global_load_lds_dwordx4 v[14:15], off nt
.Lm5s_5:
	s_add_i32 m0, s60, 0x8800
	s_nop 0
	s_cmp_eq_u32 s98, 1
	s_cbranch_scc1 .Lm5s_6
	global_load_lds_dwordx4 v[16:17], off nt
.Lm5s_6:
	s_add_i32 m0, s60, 0x8c00
	s_nop 0
	s_cmp_eq_u32 s98, 1
	s_cbranch_scc1 .Lm5s_7
	global_load_lds_dwordx4 v[18:19], off nt
.Lm5s_7:
	s_mov_b64 s[36:37], -1
	s_and_b64 vcc, exec, s[12:13]
	s_cbranch_vccnz .LBB0_198
